# phase 12: final output stores and ys row loads marked nt (streamed once); on top of v26
# speedup vs baseline: 1.0157x; 1.0157x over previous
; #define GAS __attribute__((address_space(1)))
; __device__ __forceinline__ f32x4 unpack4(u32x2 w) { return (f32x4){bflo(w.x), bfhi(w.x), bflo(w.y), bfhi(w.y)}; }
; __device__ __forceinline__ void phase12(KP kp, LAS unsigned char* lds, int wave, int bid, int G) {
;     ...
;     for (int m = bid * NWAVES + wave; m < T; m += G * NWAVES) {
;         const GAS f32x4* xr = (const GAS f32x4*)(X1 + (size_t)m * DM) + lane;
;         const i32x4 te = *(const GAS i32x4*)(TOPI + m * 4), rk = *(const GAS i32x4*)(TRANK + m * 4); const f32x4 tw = *(const GAS f32x4*)(TOPW + m * 4);
;         const i32x4 sl = (i32x4){pstart[te.x] + rk.x, pstart[te.y] + rk.y, pstart[te.z] + rk.z, pstart[te.w] + rk.w};
;         const GAS u32x2* y0 = (const GAS u32x2*)(YS + (size_t)sl.x * DM) + lane; const GAS u32x2* y1 = (const GAS u32x2*)(YS + (size_t)sl.y * DM) + lane;
;         const GAS u32x2* y2 = (const GAS u32x2*)(YS + (size_t)sl.z * DM) + lane; const GAS u32x2* y3 = (const GAS u32x2*)(YS + (size_t)sl.w * DM) + lane;
;         f32x4 v[8]; float s = 0.f;
; #pragma unroll
;         for (int j = 0; j < 8; ++j) {
;             const f32x4 mo = tw.x * unpack4(y0[64 * j]) + tw.y * unpack4(y1[64 * j]) + tw.z * unpack4(y2[64 * j]) + tw.w * unpack4(y3[64 * j]);
.LBB0_4682:
	v_lshl_add_u64 v[36:37], s[12:13], 0, v[90:91]
	s_ashr_i32 s5, s4, 31
	v_add_co_u32_e32 v104, vcc, s7, v36
	s_lshl_b64 s[0:1], s[4:5], 2
	s_nop 0
	v_addc_co_u32_e32 v105, vcc, 0, v37, vcc
	v_add_co_u32_e32 v106, vcc, s21, v36
	s_add_u32 s24, s14, s0
	s_nop 0
	v_addc_co_u32_e32 v107, vcc, 0, v37, vcc
	s_addc_u32 s25, s15, s1
	global_load_dwordx4 v[0:3], v[70:71], off
	global_load_dwordx4 v[4:7], v[70:71], off offset:1024
	global_load_dwordx4 v[8:11], v[70:71], off offset:2048
	global_load_dwordx4 v[12:15], v[70:71], off offset:3072
	global_load_dwordx4 v[16:19], v[74:75], off
	global_load_dwordx4 v[20:23], v[76:77], off
	global_load_dwordx4 v[24:27], v[78:79], off
	global_load_dwordx4 v[32:35], v[80:81], off
	global_load_dwordx4 v[28:31], v[72:73], off
	global_load_dwordx4 v[60:63], v[104:105], off offset:1024
	global_load_dwordx4 v[56:59], v[104:105], off offset:2048
	global_load_dwordx4 v[48:51], v[104:105], off offset:3072
	global_load_dwordx4 v[64:67], v[106:107], off offset:-4096
	global_load_dwordx4 v[52:55], v[106:107], off
	global_load_dwordx4 v[44:47], v[106:107], off offset:1024
	global_load_dwordx4 v[40:43], v[106:107], off offset:2048
	global_load_dwordx4 v[36:39], v[106:107], off offset:3072
	v_lshl_add_u64 v[92:93], s[8:9], 0, v[90:91]
	global_load_dwordx4 v[104:107], v100, s[24:25]
	s_add_u32 s24, s17, s0
	s_addc_u32 s25, s18, s1
	global_load_dwordx4 v[108:111], v100, s[24:25]
	s_add_u32 s0, s19, s0
	s_addc_u32 s1, s20, s1
	global_load_dwordx4 v[112:115], v100, s[0:1]
	s_add_i32 s2, s2, s6
	s_add_i32 s4, s4, s16
	s_add_u32 s8, s8, s10
	s_addc_u32 s9, s9, s11
	s_add_u32 s12, s12, s10
	s_addc_u32 s13, s13, s11
	s_cmpk_lt_i32 s2, 0x2000
	s_waitcnt vmcnt(2)
	v_lshlrev_b32_e32 v103, 2, v104
	v_lshlrev_b32_e32 v104, 2, v105
	v_lshlrev_b32_e32 v105, 2, v106
	v_lshlrev_b32_e32 v106, 2, v107
	v_add_u32_e32 v103, s3, v103
	v_add_u32_e32 v105, s3, v105
	v_add_u32_e32 v104, s3, v104
	v_add_u32_e32 v106, s3, v106
	ds_read_b32 v103, v103
	ds_read_b32 v107, v104
	ds_read_b32 v105, v105
	ds_read_b32 v116, v106
	s_waitcnt vmcnt(0)
	v_mov_b32_e32 v104, v115
	s_waitcnt lgkmcnt(3)
	v_add_u32_e32 v106, v103, v108
	s_waitcnt lgkmcnt(2)
	v_add_u32_e32 v108, v107, v109
	s_waitcnt lgkmcnt(1)
	v_add_u32_e32 v110, v105, v110
	s_waitcnt lgkmcnt(0)
	v_add_u32_e32 v116, v116, v111
	v_ashrrev_i32_e32 v107, 31, v106
	v_ashrrev_i32_e32 v109, 31, v108
	v_ashrrev_i32_e32 v111, 31, v110
	v_ashrrev_i32_e32 v117, 31, v116
	v_lshlrev_b64 v[106:107], 12, v[106:107]
	v_lshlrev_b64 v[108:109], 12, v[108:109]
	v_lshlrev_b64 v[110:111], 12, v[110:111]
	v_lshlrev_b64 v[116:117], 12, v[116:117]
	v_lshl_add_u64 v[106:107], v[68:69], 0, v[106:107]
	v_lshl_add_u64 v[108:109], v[68:69], 0, v[108:109]
	v_lshl_add_u64 v[110:111], v[68:69], 0, v[110:111]
	v_lshl_add_u64 v[116:117], v[68:69], 0, v[116:117]
	global_load_dwordx2 v[118:119], v[106:107], off nt
	global_load_dwordx2 v[120:121], v[108:109], off nt
	global_load_dwordx2 v[122:123], v[110:111], off nt
	global_load_dwordx2 v[124:125], v[116:117], off nt
	global_load_dwordx2 v[126:127], v[106:107], off offset:512 nt
	global_load_dwordx2 v[128:129], v[108:109], off offset:512 nt
	global_load_dwordx2 v[130:131], v[110:111], off offset:512 nt
	global_load_dwordx2 v[132:133], v[116:117], off offset:512 nt
	global_load_dwordx2 v[134:135], v[106:107], off offset:1024 nt
	global_load_dwordx2 v[136:137], v[108:109], off offset:1024 nt
	global_load_dwordx2 v[138:139], v[110:111], off offset:1024 nt
	global_load_dwordx2 v[140:141], v[116:117], off offset:1024 nt
	global_load_dwordx2 v[142:143], v[106:107], off offset:1536 nt
	global_load_dwordx2 v[144:145], v[108:109], off offset:1536 nt
	global_load_dwordx2 v[146:147], v[110:111], off offset:1536 nt
	global_load_dwordx2 v[148:149], v[116:117], off offset:1536 nt
	global_load_dwordx2 v[150:151], v[106:107], off offset:2048 nt
	global_load_dwordx2 v[152:153], v[106:107], off offset:2560 nt
	global_load_dwordx2 v[154:155], v[106:107], off offset:3072 nt
	s_nop 0
	global_load_dwordx2 v[106:107], v[106:107], off offset:3584 nt
	s_nop 0
	global_load_dwordx2 v[156:157], v[108:109], off offset:2048 nt
	global_load_dwordx2 v[158:159], v[108:109], off offset:2560 nt
	global_load_dwordx2 v[160:161], v[108:109], off offset:3072 nt
	s_nop 0
	global_load_dwordx2 v[108:109], v[108:109], off offset:3584 nt
	s_nop 0
	global_load_dwordx2 v[162:163], v[110:111], off offset:2048 nt
	global_load_dwordx2 v[164:165], v[110:111], off offset:2560 nt
	global_load_dwordx2 v[166:167], v[110:111], off offset:3072 nt
	s_nop 0
	global_load_dwordx2 v[110:111], v[110:111], off offset:3584 nt
	s_nop 0
	global_load_dwordx2 v[168:169], v[116:117], off offset:2048 nt
	global_load_dwordx2 v[170:171], v[116:117], off offset:2560 nt
	global_load_dwordx2 v[172:173], v[116:117], off offset:3072 nt
	s_nop 0
	global_load_dwordx2 v[116:117], v[116:117], off offset:3584 nt
	s_waitcnt vmcnt(31)
	v_lshlrev_b32_e32 v174, 16, v118
	s_waitcnt vmcnt(30)
	v_lshlrev_b32_e32 v176, 16, v120
	v_and_b32_e32 v177, 0xffff0000, v120
	v_lshlrev_b32_e32 v120, 16, v121
	v_and_b32_e32 v121, 0xffff0000, v121
	s_waitcnt vmcnt(26)
	v_lshlrev_b32_e32 v184, 16, v128
	v_and_b32_e32 v185, 0xffff0000, v128
	v_lshlrev_b32_e32 v128, 16, v129
	v_and_b32_e32 v129, 0xffff0000, v129
	v_and_b32_e32 v175, 0xffff0000, v118
	v_lshlrev_b32_e32 v118, 16, v119
	v_and_b32_e32 v119, 0xffff0000, v119
	v_lshlrev_b32_e32 v182, 16, v126
	v_and_b32_e32 v183, 0xffff0000, v126
	v_lshlrev_b32_e32 v126, 16, v127
	v_and_b32_e32 v127, 0xffff0000, v127
	s_waitcnt vmcnt(22)
	v_lshlrev_b32_e32 v192, 16, v136
	v_and_b32_e32 v193, 0xffff0000, v136
	v_lshlrev_b32_e32 v136, 16, v137
	v_and_b32_e32 v137, 0xffff0000, v137
	s_waitcnt vmcnt(18)
; #define GAS __attribute__((address_space(1)))
; __device__ __forceinline__ float dot4(f32x4 a, f32x4 b) { return (a.x * b.x + a.y * b.y) + (a.z * b.z + a.w * b.w); }
; __device__ __forceinline__ f32x4 unpack4(u32x2 w) { return (f32x4){bflo(w.x), bfhi(w.x), bflo(w.y), bfhi(w.y)}; }
; __device__ __forceinline__ void phase12(KP kp, LAS unsigned char* lds, int wave, int bid, int G) {
;     ...
;         for (int j = 0; j < 8; ++j) {
;             const f32x4 mo = tw.x * unpack4(y0[64 * j]) + tw.y * unpack4(y1[64 * j]) + tw.z * unpack4(y2[64 * j]) + tw.w * unpack4(y3[64 * j]);
;             const f32x4 g2 = *(const GAS f32x4*)(mod + 5 * 2048 + 256 * j + 4 * lane);
;             v[j] = xr[64 * j] + g2 * mo; s += dot4(v[j], v[j]); }
	v_lshlrev_b32_e32 v200, 16, v144
	v_and_b32_e32 v201, 0xffff0000, v144
	v_lshlrev_b32_e32 v144, 16, v145
	v_and_b32_e32 v145, 0xffff0000, v145
	s_waitcnt vmcnt(11)
	v_lshlrev_b32_e32 v208, 16, v156
	v_and_b32_e32 v209, 0xffff0000, v156
	v_lshlrev_b32_e32 v156, 16, v157
	v_and_b32_e32 v157, 0xffff0000, v157
	s_waitcnt vmcnt(10)
	v_lshlrev_b32_e32 v216, 16, v158
	v_and_b32_e32 v217, 0xffff0000, v158
	v_lshlrev_b32_e32 v158, 16, v159
	v_and_b32_e32 v159, 0xffff0000, v159
	s_waitcnt vmcnt(9)
	v_lshlrev_b32_e32 v224, 16, v160
	v_and_b32_e32 v225, 0xffff0000, v160
	v_lshlrev_b32_e32 v160, 16, v161
	v_and_b32_e32 v161, 0xffff0000, v161
	s_waitcnt vmcnt(8)
	v_lshlrev_b32_e32 v232, 16, v108
	v_and_b32_e32 v233, 0xffff0000, v108
	v_lshlrev_b32_e32 v108, 16, v109
	v_and_b32_e32 v109, 0xffff0000, v109
	v_pk_mul_f32 v[120:121], v[112:113], v[120:121] op_sel:[1,0]
	v_pk_mul_f32 v[176:177], v[112:113], v[176:177] op_sel:[1,0]
	v_pk_mul_f32 v[128:129], v[112:113], v[128:129] op_sel:[1,0]
	v_pk_mul_f32 v[184:185], v[112:113], v[184:185] op_sel:[1,0]
	v_lshlrev_b32_e32 v178, 16, v122
	v_and_b32_e32 v179, 0xffff0000, v122
	v_lshlrev_b32_e32 v122, 16, v123
	v_and_b32_e32 v123, 0xffff0000, v123
	v_lshlrev_b32_e32 v186, 16, v130
	v_and_b32_e32 v187, 0xffff0000, v130
	v_lshlrev_b32_e32 v130, 16, v131
	v_and_b32_e32 v131, 0xffff0000, v131
	v_lshlrev_b32_e32 v190, 16, v134
	v_and_b32_e32 v191, 0xffff0000, v134
	v_lshlrev_b32_e32 v134, 16, v135
	v_and_b32_e32 v135, 0xffff0000, v135
	v_lshlrev_b32_e32 v198, 16, v142
	v_and_b32_e32 v199, 0xffff0000, v142
	v_lshlrev_b32_e32 v142, 16, v143
	v_and_b32_e32 v143, 0xffff0000, v143
	v_lshlrev_b32_e32 v206, 16, v150
	v_and_b32_e32 v207, 0xffff0000, v150
	v_lshlrev_b32_e32 v150, 16, v151
	v_and_b32_e32 v151, 0xffff0000, v151
	v_lshlrev_b32_e32 v214, 16, v152
	v_and_b32_e32 v215, 0xffff0000, v152
	v_lshlrev_b32_e32 v152, 16, v153
	v_and_b32_e32 v153, 0xffff0000, v153
	v_lshlrev_b32_e32 v222, 16, v154
	v_and_b32_e32 v223, 0xffff0000, v154
	v_lshlrev_b32_e32 v154, 16, v155
	v_and_b32_e32 v155, 0xffff0000, v155
	v_lshlrev_b32_e32 v230, 16, v106
	v_and_b32_e32 v231, 0xffff0000, v106
	v_lshlrev_b32_e32 v106, 16, v107
	v_and_b32_e32 v107, 0xffff0000, v107
	v_pk_mul_f32 v[192:193], v[112:113], v[192:193] op_sel:[1,0]
	v_pk_mul_f32 v[136:137], v[112:113], v[136:137] op_sel:[1,0]
	v_pk_mul_f32 v[144:145], v[112:113], v[144:145] op_sel:[1,0]
	v_pk_mul_f32 v[200:201], v[112:113], v[200:201] op_sel:[1,0]
	v_pk_mul_f32 v[156:157], v[112:113], v[156:157] op_sel:[1,0]
	v_pk_mul_f32 v[208:209], v[112:113], v[208:209] op_sel:[1,0]
	v_pk_mul_f32 v[216:217], v[112:113], v[216:217] op_sel:[1,0]
	v_pk_mul_f32 v[158:159], v[112:113], v[158:159] op_sel:[1,0]
	v_pk_mul_f32 v[160:161], v[112:113], v[160:161] op_sel:[1,0]
	v_pk_mul_f32 v[224:225], v[112:113], v[224:225] op_sel:[1,0]
	v_pk_mul_f32 v[108:109], v[112:113], v[108:109] op_sel:[1,0]
	v_pk_mul_f32 v[232:233], v[112:113], v[232:233] op_sel:[1,0]
	v_pk_fma_f32 v[174:175], v[112:113], v[174:175], v[176:177] op_sel_hi:[0,1,1]
	v_pk_fma_f32 v[118:119], v[112:113], v[118:119], v[120:121] op_sel_hi:[0,1,1]
	v_pk_fma_f32 v[120:121], v[112:113], v[182:183], v[184:185] op_sel_hi:[0,1,1]
	v_pk_fma_f32 v[126:127], v[112:113], v[126:127], v[128:129] op_sel_hi:[0,1,1]
	v_lshlrev_b32_e32 v180, 16, v124
	v_and_b32_e32 v181, 0xffff0000, v124
	v_lshlrev_b32_e32 v124, 16, v125
	v_and_b32_e32 v125, 0xffff0000, v125
	v_lshlrev_b32_e32 v188, 16, v132
	v_and_b32_e32 v189, 0xffff0000, v132
	v_lshlrev_b32_e32 v132, 16, v133
	v_and_b32_e32 v133, 0xffff0000, v133
	v_lshlrev_b32_e32 v194, 16, v138
	v_and_b32_e32 v195, 0xffff0000, v138
	v_lshlrev_b32_e32 v138, 16, v139
	v_and_b32_e32 v139, 0xffff0000, v139
	v_lshlrev_b32_e32 v202, 16, v146
	v_and_b32_e32 v203, 0xffff0000, v146
	v_lshlrev_b32_e32 v146, 16, v147
	v_and_b32_e32 v147, 0xffff0000, v147
	s_waitcnt vmcnt(7)
	v_lshlrev_b32_e32 v210, 16, v162
	v_and_b32_e32 v211, 0xffff0000, v162
	v_lshlrev_b32_e32 v162, 16, v163
	v_and_b32_e32 v163, 0xffff0000, v163
	s_waitcnt vmcnt(6)
	v_lshlrev_b32_e32 v218, 16, v164
	v_and_b32_e32 v219, 0xffff0000, v164
	v_lshlrev_b32_e32 v164, 16, v165
	v_and_b32_e32 v165, 0xffff0000, v165
	s_waitcnt vmcnt(5)
	v_lshlrev_b32_e32 v226, 16, v166
	v_and_b32_e32 v227, 0xffff0000, v166
	v_lshlrev_b32_e32 v166, 16, v167
	v_and_b32_e32 v167, 0xffff0000, v167
	s_waitcnt vmcnt(4)
	v_lshlrev_b32_e32 v234, 16, v110
	v_and_b32_e32 v235, 0xffff0000, v110
	v_lshlrev_b32_e32 v110, 16, v111
	v_and_b32_e32 v111, 0xffff0000, v111
	v_pk_fma_f32 v[128:129], v[112:113], v[134:135], v[136:137] op_sel_hi:[0,1,1]
	v_pk_fma_f32 v[134:135], v[112:113], v[190:191], v[192:193] op_sel_hi:[0,1,1]
	v_pk_fma_f32 v[136:137], v[112:113], v[198:199], v[200:201] op_sel_hi:[0,1,1]
	v_pk_fma_f32 v[142:143], v[112:113], v[142:143], v[144:145] op_sel_hi:[0,1,1]
	v_pk_fma_f32 v[144:145], v[112:113], v[206:207], v[208:209] op_sel_hi:[0,1,1]
	v_pk_fma_f32 v[150:151], v[112:113], v[150:151], v[156:157] op_sel_hi:[0,1,1]
	v_pk_fma_f32 v[152:153], v[112:113], v[152:153], v[158:159] op_sel_hi:[0,1,1]
	v_pk_fma_f32 v[156:157], v[112:113], v[214:215], v[216:217] op_sel_hi:[0,1,1]
	v_pk_fma_f32 v[158:159], v[112:113], v[222:223], v[224:225] op_sel_hi:[0,1,1]
	v_pk_fma_f32 v[154:155], v[112:113], v[154:155], v[160:161] op_sel_hi:[0,1,1]
	v_pk_fma_f32 v[160:161], v[112:113], v[230:231], v[232:233] op_sel_hi:[0,1,1]
	v_pk_fma_f32 v[106:107], v[112:113], v[106:107], v[108:109] op_sel_hi:[0,1,1]
	v_pk_fma_f32 v[108:109], v[114:115], v[122:123], v[118:119] op_sel_hi:[0,1,1]
	v_pk_fma_f32 v[112:113], v[114:115], v[178:179], v[174:175] op_sel_hi:[0,1,1]
	v_pk_fma_f32 v[118:119], v[114:115], v[130:131], v[126:127] op_sel_hi:[0,1,1]
	v_pk_fma_f32 v[120:121], v[114:115], v[186:187], v[120:121] op_sel_hi:[0,1,1]
	v_lshlrev_b32_e32 v196, 16, v140
	v_and_b32_e32 v197, 0xffff0000, v140
	v_lshlrev_b32_e32 v140, 16, v141
	v_and_b32_e32 v141, 0xffff0000, v141
	v_lshlrev_b32_e32 v204, 16, v148
	v_and_b32_e32 v205, 0xffff0000, v148
	v_lshlrev_b32_e32 v148, 16, v149
	v_and_b32_e32 v149, 0xffff0000, v149
	s_waitcnt vmcnt(3)
; #define GAS __attribute__((address_space(1)))
; __device__ __forceinline__ float dot4(f32x4 a, f32x4 b) { return (a.x * b.x + a.y * b.y) + (a.z * b.z + a.w * b.w); }
; __device__ __forceinline__ f32x4 unpack4(u32x2 w) { return (f32x4){bflo(w.x), bfhi(w.x), bflo(w.y), bfhi(w.y)}; }
; __device__ __forceinline__ void phase12(KP kp, LAS unsigned char* lds, int wave, int bid, int G) {
;     ...
;         for (int j = 0; j < 8; ++j) {
;             const f32x4 mo = tw.x * unpack4(y0[64 * j]) + tw.y * unpack4(y1[64 * j]) + tw.z * unpack4(y2[64 * j]) + tw.w * unpack4(y3[64 * j]);
;             const f32x4 g2 = *(const GAS f32x4*)(mod + 5 * 2048 + 256 * j + 4 * lane);
;             v[j] = xr[64 * j] + g2 * mo; s += dot4(v[j], v[j]); }
	v_lshlrev_b32_e32 v212, 16, v168
	v_and_b32_e32 v213, 0xffff0000, v168
	v_lshlrev_b32_e32 v168, 16, v169
	v_and_b32_e32 v169, 0xffff0000, v169
	s_waitcnt vmcnt(2)
	v_lshlrev_b32_e32 v220, 16, v170
	v_and_b32_e32 v221, 0xffff0000, v170
	v_lshlrev_b32_e32 v170, 16, v171
	v_and_b32_e32 v171, 0xffff0000, v171
	s_waitcnt vmcnt(1)
	v_lshlrev_b32_e32 v228, 16, v172
	v_and_b32_e32 v229, 0xffff0000, v172
	v_lshlrev_b32_e32 v172, 16, v173
	v_and_b32_e32 v173, 0xffff0000, v173
	s_waitcnt vmcnt(0)
	v_lshlrev_b32_e32 v236, 16, v116
	v_and_b32_e32 v237, 0xffff0000, v116
	v_lshlrev_b32_e32 v116, 16, v117
	v_and_b32_e32 v117, 0xffff0000, v117
	v_pk_fma_f32 v[122:123], v[114:115], v[194:195], v[134:135] op_sel_hi:[0,1,1]
	v_pk_fma_f32 v[126:127], v[114:115], v[138:139], v[128:129] op_sel_hi:[0,1,1]
	v_pk_fma_f32 v[128:129], v[114:115], v[146:147], v[142:143] op_sel_hi:[0,1,1]
	v_pk_fma_f32 v[130:131], v[114:115], v[202:203], v[136:137] op_sel_hi:[0,1,1]
	v_pk_fma_f32 v[134:135], v[114:115], v[162:163], v[150:151] op_sel_hi:[0,1,1]
	v_pk_fma_f32 v[136:137], v[114:115], v[210:211], v[144:145] op_sel_hi:[0,1,1]
	v_pk_fma_f32 v[138:139], v[114:115], v[218:219], v[156:157] op_sel_hi:[0,1,1]
	v_pk_fma_f32 v[142:143], v[114:115], v[164:165], v[152:153] op_sel_hi:[0,1,1]
	v_pk_fma_f32 v[144:145], v[114:115], v[166:167], v[154:155] op_sel_hi:[0,1,1]
	v_pk_fma_f32 v[146:147], v[114:115], v[226:227], v[158:159] op_sel_hi:[0,1,1]
	v_pk_fma_f32 v[106:107], v[114:115], v[110:111], v[106:107] op_sel_hi:[0,1,1]
	v_pk_fma_f32 v[110:111], v[114:115], v[234:235], v[160:161] op_sel_hi:[0,1,1]
	v_pk_fma_f32 v[112:113], v[104:105], v[180:181], v[112:113] op_sel_hi:[0,1,1]
	v_pk_fma_f32 v[108:109], v[104:105], v[124:125], v[108:109] op_sel_hi:[0,1,1]
	v_pk_fma_f32 v[114:115], v[104:105], v[188:189], v[120:121] op_sel_hi:[0,1,1]
	v_pk_fma_f32 v[118:119], v[104:105], v[132:133], v[118:119] op_sel_hi:[0,1,1]
	v_pk_fma_f32 v[120:121], v[104:105], v[140:141], v[126:127] op_sel_hi:[0,1,1]
	v_pk_fma_f32 v[122:123], v[104:105], v[196:197], v[122:123] op_sel_hi:[0,1,1]
	v_pk_fma_f32 v[124:125], v[104:105], v[204:205], v[130:131] op_sel_hi:[0,1,1]
	v_pk_fma_f32 v[126:127], v[104:105], v[148:149], v[128:129] op_sel_hi:[0,1,1]
	v_pk_fma_f32 v[128:129], v[104:105], v[212:213], v[136:137] op_sel_hi:[0,1,1]
	v_pk_fma_f32 v[130:131], v[104:105], v[168:169], v[134:135] op_sel_hi:[0,1,1]
	v_pk_fma_f32 v[132:133], v[104:105], v[170:171], v[142:143] op_sel_hi:[0,1,1]
	v_pk_fma_f32 v[134:135], v[104:105], v[220:221], v[138:139] op_sel_hi:[0,1,1]
	v_pk_fma_f32 v[136:137], v[104:105], v[228:229], v[146:147] op_sel_hi:[0,1,1]
	v_pk_fma_f32 v[138:139], v[104:105], v[172:173], v[144:145] op_sel_hi:[0,1,1]
	v_pk_fma_f32 v[110:111], v[104:105], v[236:237], v[110:111] op_sel_hi:[0,1,1]
	v_pk_fma_f32 v[104:105], v[104:105], v[116:117], v[106:107] op_sel_hi:[0,1,1]
	v_pk_fma_f32 v[2:3], v[2:3], v[108:109], v[66:67]
	v_pk_fma_f32 v[0:1], v[0:1], v[112:113], v[64:65]
	v_pk_fma_f32 v[6:7], v[6:7], v[118:119], v[62:63]
	v_pk_fma_f32 v[4:5], v[4:5], v[114:115], v[60:61]
	v_pk_fma_f32 v[8:9], v[8:9], v[122:123], v[56:57]
	v_pk_fma_f32 v[10:11], v[10:11], v[120:121], v[58:59]
	v_pk_fma_f32 v[26:27], v[26:27], v[138:139], v[42:43]
	v_pk_fma_f32 v[34:35], v[34:35], v[104:105], v[38:39]
	v_mov_b32_e32 v38, v1
	v_mov_b32_e32 v39, v5
	v_mov_b32_e32 v42, v3
	v_mov_b32_e32 v43, v7
	v_pk_fma_f32 v[20:21], v[20:21], v[134:135], v[44:45]
	v_pk_fma_f32 v[22:23], v[22:23], v[132:133], v[46:47]
	v_pk_fma_f32 v[24:25], v[24:25], v[136:137], v[40:41]
	v_pk_fma_f32 v[32:33], v[32:33], v[110:111], v[36:37]
	v_mov_b32_e32 v36, v0
	v_mov_b32_e32 v37, v4
	v_mov_b32_e32 v40, v2
	v_mov_b32_e32 v41, v6
	v_pk_mul_f32 v[44:45], v[10:11], v[10:11]
	v_pk_mul_f32 v[46:47], v[8:9], v[8:9]
	v_pk_mul_f32 v[38:39], v[38:39], v[38:39]
	v_pk_mul_f32 v[42:43], v[42:43], v[42:43]
	v_pk_fma_f32 v[14:15], v[14:15], v[126:127], v[50:51]
	v_pk_fma_f32 v[12:13], v[12:13], v[124:125], v[48:49]
	v_pk_mov_b32 v[60:61], v[46:47], v[44:45] op_sel:[1,0]
	v_mov_b32_e32 v47, v45
	v_pk_fma_f32 v[36:37], v[36:37], v[36:37], v[38:39]
	v_pk_fma_f32 v[38:39], v[40:41], v[40:41], v[42:43]
	v_pk_fma_f32 v[18:19], v[18:19], v[130:131], v[54:55]
	v_pk_fma_f32 v[16:17], v[16:17], v[128:129], v[52:53]
	v_mul_f32_e32 v48, v13, v13
	v_mul_f32_e32 v50, v15, v15
	v_pk_add_f32 v[40:41], v[60:61], v[46:47]
	v_pk_add_f32 v[36:37], v[36:37], v[38:39]
	v_mul_f32_e32 v59, v16, v16
	v_mul_f32_e32 v62, v17, v17
	v_mul_f32_e32 v63, v18, v18
	v_mul_f32_e32 v64, v19, v19
	v_pk_fma_f32 v[44:45], v[12:13], v[12:13], v[48:49] op_sel_hi:[1,1,0]
	v_pk_fma_f32 v[48:49], v[14:15], v[14:15], v[50:51] op_sel_hi:[1,1,0]
	v_pk_add_f32 v[38:39], v[40:41], v[40:41] op_sel:[0,1] op_sel_hi:[1,0]
	v_pk_add_f32 v[36:37], v[36:37], v[36:37] op_sel:[0,1] op_sel_hi:[1,0]
	v_pk_mul_f32 v[52:53], v[22:23], v[22:23]
	v_pk_mul_f32 v[54:55], v[20:21], v[20:21]
	v_mov_b32_e32 v45, v63
	v_mov_b32_e32 v49, v64
	v_mov_b32_e32 v39, v62
	v_mov_b32_e32 v37, v59
	v_pk_mov_b32 v[50:51], v[54:55], v[52:53] op_sel:[1,0]
; #define GAS __attribute__((address_space(1)))
; __device__ __forceinline__ float wave_sum(float v) {
; #pragma unroll
;     for (int o = 1; o < 64; o <<= 1) v += __shfl_xor(v, o);
;     return v;
; }
; __device__ __forceinline__ void phase12(KP kp, LAS unsigned char* lds, int wave, int bid, int G) {
;     ...
;         const float rstd = 1.0f / sqrtf(wave_sum(s) * (1.0f / DM) + EPS);
;         GAS f32x4* o = (GAS f32x4*)(KOUT() + (size_t)m * DM) + lane;
; #pragma unroll
;         for (int j = 0; j < 8; ++j) o[64 * j] = v[j] * rstd * *(const GAS f32x4*)(fg + 256 * j + 4 * lane);
	v_mov_b32_e32 v55, v53
	v_pk_add_f32 v[40:41], v[44:45], v[48:49]
	v_pk_add_f32 v[36:37], v[36:37], v[38:39]
	v_mul_f32_e32 v56, v25, v25
	v_mul_f32_e32 v58, v27, v27
	v_pk_add_f32 v[42:43], v[50:51], v[54:55]
	v_pk_add_f32 v[36:37], v[36:37], v[40:41]
	v_mul_f32_e32 v65, v32, v32
	v_mul_f32_e32 v66, v33, v33
	v_mul_f32_e32 v67, v34, v34
	v_mul_f32_e32 v103, v35, v35
	v_pk_fma_f32 v[52:53], v[24:25], v[24:25], v[56:57] op_sel_hi:[1,1,0]
	v_pk_fma_f32 v[56:57], v[26:27], v[26:27], v[58:59] op_sel_hi:[1,1,0]
	v_pk_add_f32 v[42:43], v[42:43], v[42:43] op_sel:[0,1] op_sel_hi:[1,0]
	v_pk_add_f32 v[36:37], v[36:37], v[36:37] op_sel:[0,1] op_sel_hi:[1,0]
	v_mov_b32_e32 v53, v67
	v_mov_b32_e32 v57, v103
	v_mov_b32_e32 v43, v66
	v_mov_b32_e32 v37, v65
	v_pk_add_f32 v[44:45], v[52:53], v[56:57]
	v_pk_add_f32 v[36:37], v[36:37], v[42:43]
	s_nop 0
	v_pk_add_f32 v[36:37], v[36:37], v[44:45]
	s_nop 0
	v_add_f32_e32 v36, v36, v37
	s_nop 1
	v_add_f32_dpp v36, v36, v36 quad_perm:[1,0,3,2] row_mask:0xf bank_mask:0xf
	s_nop 1
	v_add_f32_dpp v36, v36, v36 quad_perm:[2,3,0,1] row_mask:0xf bank_mask:0xf
	s_nop 1
	v_add_f32_dpp v36, v36, v36 row_half_mirror row_mask:0xf bank_mask:0xf
	s_nop 1
	v_add_f32_dpp v36, v36, v36 row_mirror row_mask:0xf bank_mask:0xf
	v_mov_b32_e32 v37, v36
	s_nop 1
	v_permlane16_swap_b32_e32 v36, v37
	v_add_f32_e32 v36, v36, v37
	v_mov_b32_e32 v37, v36
	s_nop 1
	v_permlane32_swap_b32_e32 v36, v37
	v_add_f32_e32 v36, v36, v37
	global_load_dwordx4 v[44:47], v[72:73], off offset:1024
	global_load_dwordx4 v[48:51], v[72:73], off offset:2048
	global_load_dwordx4 v[52:55], v[72:73], off offset:3072
	global_load_dwordx4 v[56:59], v[82:83], off
	global_load_dwordx4 v[60:63], v[84:85], off
	global_load_dwordx4 v[64:67], v[86:87], off
	global_load_dwordx4 v[94:97], v[88:89], off
	v_fmamk_f32 v36, v36, 0x3a000000, v101
	v_mul_f32_e32 v37, 0x4f800000, v36
	v_cmp_gt_f32_e32 vcc, s22, v36
	s_nop 1
	v_cndmask_b32_e32 v36, v36, v37, vcc
	v_sqrt_f32_e32 v37, v36
	s_nop 0
	v_add_u32_e32 v38, -1, v37
	v_add_u32_e32 v39, 1, v37
	v_fma_f32 v40, -v38, v37, v36
	v_fma_f32 v41, -v39, v37, v36
	v_cmp_ge_f32_e64 s[0:1], 0, v40
	s_nop 1
	v_cndmask_b32_e64 v37, v37, v38, s[0:1]
	v_cmp_lt_f32_e64 s[0:1], 0, v41
	s_nop 1
	v_cndmask_b32_e64 v37, v37, v39, s[0:1]
	v_mul_f32_e32 v38, 0x37800000, v37
	v_cndmask_b32_e32 v37, v37, v38, vcc
	v_cmp_class_f32_e32 vcc, v36, v102
	s_nop 1
	v_cndmask_b32_e32 v36, v37, v36, vcc
	v_div_scale_f32 v37, s[0:1], v36, v36, 1.0
	v_rcp_f32_e32 v39, v37
	v_div_scale_f32 v38, vcc, 1.0, v36, 1.0
	v_fma_f32 v40, -v37, v39, 1.0
	v_fmac_f32_e32 v39, v40, v39
	v_mul_f32_e32 v40, v38, v39
	v_fma_f32 v41, -v37, v40, v38
	v_fmac_f32_e32 v40, v41, v39
	v_fma_f32 v37, -v37, v40, v38
	v_div_fmas_f32 v37, v37, v39, v40
	v_div_fixup_f32 v36, v37, v36, 1.0
	v_add_co_u32_e32 v38, vcc, s23, v92
	s_nop 1
	v_addc_co_u32_e32 v39, vcc, 0, v93, vcc
	s_waitcnt vmcnt(0)
	v_pk_mul_f32 v[0:1], v[0:1], v[36:37] op_sel_hi:[1,0]
	v_pk_mul_f32 v[2:3], v[2:3], v[36:37] op_sel_hi:[1,0]
	v_pk_mul_f32 v[0:1], v[28:29], v[0:1]
	v_pk_mul_f32 v[2:3], v[30:31], v[2:3]
	global_store_dwordx4 v[92:93], v[0:3], off nt
	v_pk_mul_f32 v[4:5], v[4:5], v[36:37] op_sel_hi:[1,0]
	v_pk_mul_f32 v[6:7], v[6:7], v[36:37] op_sel_hi:[1,0]
	v_pk_mul_f32 v[4:5], v[44:45], v[4:5]
	v_pk_mul_f32 v[6:7], v[46:47], v[6:7]
	global_store_dwordx4 v[92:93], v[4:7], off offset:1024 nt
	v_pk_mul_f32 v[8:9], v[8:9], v[36:37] op_sel_hi:[1,0]
	v_pk_mul_f32 v[10:11], v[10:11], v[36:37] op_sel_hi:[1,0]
	v_pk_mul_f32 v[8:9], v[48:49], v[8:9]
	v_pk_mul_f32 v[10:11], v[50:51], v[10:11]
	global_store_dwordx4 v[92:93], v[8:11], off offset:2048 nt
	v_pk_mul_f32 v[12:13], v[12:13], v[36:37] op_sel_hi:[1,0]
	v_pk_mul_f32 v[14:15], v[14:15], v[36:37] op_sel_hi:[1,0]
	v_pk_mul_f32 v[12:13], v[52:53], v[12:13]
	v_pk_mul_f32 v[14:15], v[54:55], v[14:15]
	global_store_dwordx4 v[92:93], v[12:15], off offset:3072 nt
	v_pk_mul_f32 v[16:17], v[16:17], v[36:37] op_sel_hi:[1,0]
	v_pk_mul_f32 v[18:19], v[18:19], v[36:37] op_sel_hi:[1,0]
	v_pk_mul_f32 v[16:17], v[56:57], v[16:17]
	v_pk_mul_f32 v[18:19], v[58:59], v[18:19]
	global_store_dwordx4 v[38:39], v[16:19], off nt
	v_pk_mul_f32 v[20:21], v[20:21], v[36:37] op_sel_hi:[1,0]
	v_pk_mul_f32 v[22:23], v[22:23], v[36:37] op_sel_hi:[1,0]
	v_pk_mul_f32 v[20:21], v[60:61], v[20:21]
	v_pk_mul_f32 v[22:23], v[62:63], v[22:23]
	global_store_dwordx4 v[38:39], v[20:23], off offset:1024 nt
	v_pk_mul_f32 v[24:25], v[24:25], v[36:37] op_sel_hi:[1,0]
	v_pk_mul_f32 v[26:27], v[26:27], v[36:37] op_sel_hi:[1,0]
	v_pk_mul_f32 v[24:25], v[64:65], v[24:25]
	v_pk_mul_f32 v[26:27], v[66:67], v[26:27]
	global_store_dwordx4 v[38:39], v[24:27], off offset:2048 nt
	v_pk_mul_f32 v[32:33], v[32:33], v[36:37] op_sel_hi:[1,0]
	v_pk_mul_f32 v[34:35], v[34:35], v[36:37] op_sel_hi:[1,0]
	v_pk_mul_f32 v[32:33], v[94:95], v[32:33]
	v_pk_mul_f32 v[34:35], v[96:97], v[34:35]
	global_store_dwordx4 v[38:39], v[32:35], off offset:3072 nt
	s_cbranch_scc1 .LBB0_4682
